# v47 plus LDS-free item conversion in the barrier-wait work loop after the diff / neighbourhood attention phase
# speedup vs baseline: 1.0138x; 1.0138x over previous
; #define LAS __attribute__((address_space(3)))
; __device__ __forceinline__ unsigned xb_ld(unsigned* p)              { return __hip_atomic_load(p, __ATOMIC_RELAXED, __HIP_MEMORY_SCOPE_AGENT); }
; __device__ __forceinline__ unsigned xb_add(unsigned* p, unsigned v) { return __hip_atomic_fetch_add(p, v, __ATOMIC_RELAXED, __HIP_MEMORY_SCOPE_AGENT); }
;     __device__ __forceinline__ unsigned char* ws() const { return *(unsigned char* const __attribute__((address_space(4)))*)(p + 232); }
; __device__ __forceinline__ void xcd_barrier_work(const XcdBarrier& b, const KA& a, unsigned char* ws, LAS unsigned char* lds) {
;     ...
;     int tl = tid_x(); asm volatile("" : "+v"(tl));
;     const int wave = __builtin_amdgcn_readfirstlane(tl >> 6), lane = tl & 63;
;     LAS float* scr = (LAS float*)(lds + wave * 16640);
;     unsigned spins = 0;
;     while (st[4] == 0u) {
;         if (tl == 0) {
;             if (xb_ld(&bar[XB_XGEN(b.x)]) != st[5] || xb_ld(&bar[XB_TMO]) != 0u) {
;                 __builtin_amdgcn_fence(__ATOMIC_ACQUIRE, "agent");
;                 asm volatile("s_waitcnt vmcnt(0)" ::: "memory");
;                 st[4] = 1u;
;             } else {
;                 if (++spins > XB_SPIN_CAP) atomicAdd(&bar[XB_TMO], 1u);
;                 unsigned base = 0xFFFFFFFFu;
;                 if (st[7] == 0u) { base = xb_add(qw, 8u); if (base >= (unsigned)Q_TOTAL) st[7] = 1u; }
;                 st[6] = base;
;             }
;         }
;         __syncthreads();
;         if (st[4] != 0u) break;
;         const unsigned base = st[6];
;         if (base < (unsigned)Q_TOTAL) { if (base + wave < (unsigned)Q_TOTAL) conv_expert_item(a, ws, (int)base + wave, scr, lane); }
.LBB0_622:
	s_ashr_i32 s18, s0, 6
	v_lshlrev_b32_e32 v1, 2, v0
	s_add_u32 s10, s8, 0x20000
	s_mul_i32 s0, s18, 0x4100
	v_bfe_u32 v9, v0, 4, 2
	v_and_b32_e32 v2, 60, v1
	s_addc_u32 s11, s9, 0
	s_add_i32 s0, s0, 0
	v_mul_u32_u24_e32 v1, 0x104, v9
	v_lshlrev_b32_e32 v3, 2, v2
	v_add3_u32 v10, s0, v1, v3
	v_and_b32_e32 v1, 7, v0
	v_bfe_u32 v11, v0, 3, 3
	v_cmp_eq_u32_e64 s[2:3], 0, v0
	s_add_u32 s19, s8, 0x32000000
	v_lshlrev_b32_e32 v4, 3, v1
	v_mul_u32_u24_e32 v0, 0x820, v1
	v_lshlrev_b32_e32 v1, 2, v11
	s_addc_u32 s20, s9, 0
	v_add3_u32 v12, s0, v0, v1
	s_lshl_b32 s0, s73, 2
	s_add_u32 s0, s6, s0
	s_addc_u32 s1, s7, 0
	s_add_u32 s8, s0, 0x2400
	v_mov_b32_e32 v8, 0
	v_mov_b32_e32 v5, v193
	v_or_b32_e32 v13, 8, v11
	v_or_b32_e32 v14, 16, v11
	v_or_b32_e32 v15, 24, v11
	v_or_b32_e32 v16, 32, v11
	v_or_b32_e32 v17, 40, v11
	v_or_b32_e32 v18, 48, v11
	v_or_b32_e32 v19, 56, v11
	s_addc_u32 s9, s1, 0
	v_lshlrev_b32_e32 v6, 2, v2
	s_branch .LBB0_627
.LBB0_625:
	v_readlane_b32 s0, v254, 24
	s_barrier
	s_nop 0
	v_mov_b32_e32 v0, s0
	ds_read_b32 v0, v0
	s_waitcnt lgkmcnt(0)
	v_cmp_ne_u32_e64 s[0:1], 0, v0

; __device__ __forceinline__ CvtDesc conv_expert_desc(const KA& a, unsigned char* ws, int q) {
;     const int l = q / Q_PER_L; int r = q - l * Q_PER_L;
;     unsigned char* wl = ws + WS_W + (size_t)l * W_LSTRIDE;
;     CvtDesc d; d.f8 = (MOE_FP8_LAST && (MOE_FP8_GU_ALL || l == NLAYER - 1)) ? 1 : 0;
;     if (MOE_FP8_LAST && MOE_FP8_DOWN_ALL && r >= 2 * Q_IG) d.f8 = 1;
;     const int eb = d.f8 ? 1 : 2;
;     if (r < 2 * Q_IG) { const int up = r >= Q_IG; if (up) r -= Q_IG; const int e = r >> 8, rr = r & 255, kb = rr >> 3, nb = rr & 7, n0 = nb * 64;
;         const float* src = e < 64 ? a.in(up ? 21 : 20) + ((size_t)l * 64 + e) * DM * FFE : a.in(up ? 24 : 23) + (size_t)l * DM * FFE;
;         d.src = src + (size_t)(kb * 64) * FFE + n0; d.N = FFE; d.dKB = DM * eb;
;         d.dst = wl + W_GU + ((size_t)e * 1024 * DM + (size_t)((n0 >> 7) * 256 + up * 128 + (n0 & 127)) * DM + kb * 64) * eb;
;     } else { r -= 2 * Q_IG; const int e = r >> 8, rr = r & 255, kb = rr >> 5, nb = rr & 31;
;         const float* src = e < 64 ? a.in(22) + ((size_t)l * 64 + e) * FFE * DM : a.in(25) + (size_t)l * FFE * DM;
;         d.src = src + (size_t)(kb * 64) * DM + nb * 64; d.N = DM; d.dKB = FFE * eb;
;         d.dst = wl + W_D + ((size_t)e * DM * FFE + (size_t)(nb * 64) * FFE + kb * 64) * eb; }
;     return d;
; }
; __device__ __forceinline__ void xcd_barrier_work(const XcdBarrier& b, const KA& a, unsigned char* ws, LAS unsigned char* lds) {
;     ...
;     while (st[4] == 0u) {
;         if (tl == 0) {
;             if (xb_ld(&bar[XB_XGEN(b.x)]) != st[5] || xb_ld(&bar[XB_TMO]) != 0u) {
;                 __builtin_amdgcn_fence(__ATOMIC_ACQUIRE, "agent");
;                 asm volatile("s_waitcnt vmcnt(0)" ::: "memory");
;                 st[4] = 1u;
;             } else {
;                 if (++spins > XB_SPIN_CAP) atomicAdd(&bar[XB_TMO], 1u);
;                 unsigned base = 0xFFFFFFFFu;
;                 if (st[7] == 0u) { base = xb_add(qw, 8u); if (base >= (unsigned)Q_TOTAL) st[7] = 1u; }
;                 st[6] = base;
;             }
;         }
;         __syncthreads();
;         if (st[4] != 0u) break;
;         const unsigned base = st[6];
;         if (base < (unsigned)Q_TOTAL) { if (base + wave < (unsigned)Q_TOTAL) conv_expert_item(a, ws, (int)base + wave, scr, lane); }
.LBB0_646:
	s_andn2_b64 vcc, exec, s[0:1]
	s_cbranch_vccnz .LBB0_625
	s_add_i32 s24, s24, s18
	s_cmp_gt_u32 s24, 0x185ff
	s_cbranch_scc1 .LBB0_625
	s_cmp_ge_u32 s24, 0xc300
	s_cselect_b32 s21, 1, 0
	s_cselect_b32 s0, 0xc300, 0
	s_sub_u32 s24, s24, s0
	s_cmp_ge_u32 s24, 0x8200
	s_cbranch_scc1 .Lbw_dn
	s_cmp_ge_u32 s24, 0x4100
	s_cselect_b32 s22, 1, 0
	s_cselect_b32 s0, 0x4100, 0
	s_sub_u32 s24, s24, s0
	s_lshr_b32 s23, s24, 8
	s_lshl_b32 s17, s21, 6
	s_add_u32 s17, s17, s23
	s_cmp_eq_u32 s23, 64
	s_cselect_b32 s0, 3, 0
	s_cselect_b32 s17, s21, s17
	s_add_u32 s0, s0, s22
	s_lshl_b32 s0, s0, 3
	s_add_u32 s0, s0, 0xa0
	s_load_dwordx2 s[12:13], s[76:77], s0
	s_lshr_b32 s68, s24, 3
	s_and_b32 s68, s68, 31
	s_and_b32 s16, s24, 7
	s_lshl_b32 s0, s68, 17
	s_lshl_b32 s1, s16, 8
	s_or_b32 s0, s0, s1
	s_lshl_b32 s1, s17, 22
	s_or_b32 s0, s0, s1
	s_lshr_b32 s1, s17, 10
	s_waitcnt lgkmcnt(0)
	s_add_u32 s12, s12, s0
	s_addc_u32 s13, s13, s1
	s_lshr_b32 s0, s16, 1
	s_lshl_b32 s0, s0, 8
	s_lshl_b32 s1, s22, 7
	s_add_u32 s0, s0, s1
	s_and_b32 s1, s16, 1
	s_lshl_b32 s1, s1, 6
	s_add_u32 s0, s0, s1
	s_lshl_b32 s0, s0, 11
	s_lshl_b32 s1, s68, 6
	s_add_u32 s0, s0, s1
	s_lshl_b32 s1, s23, 21
	s_add_u32 s0, s0, s1
	s_add_u32 s0, s0, 0x2000000
	s_mul_i32 s1, s21, 0x1a800000
	s_add_u32 s0, s0, s1
	s_add_u32 s14, s19, s0
	s_addc_u32 s15, s20, 0
	s_mov_b32 s16, 0
	s_branch .Lbw_dd
.Lbw_dn:
	s_sub_u32 s24, s24, 0x8200
	s_lshr_b32 s23, s24, 8
	s_lshl_b32 s17, s21, 6
	s_add_u32 s17, s17, s23
	s_cmp_eq_u32 s23, 64
	s_cselect_b32 s0, 5, 2
	s_cselect_b32 s17, s21, s17
	s_lshl_b32 s0, s0, 3
	s_add_u32 s0, s0, 0xa0
	s_load_dwordx2 s[12:13], s[76:77], s0
	s_lshr_b32 s68, s24, 5
	s_and_b32 s68, s68, 7
	s_and_b32 s16, s24, 31
	s_lshl_b32 s0, s68, 19
	s_lshl_b32 s1, s16, 8
	s_or_b32 s0, s0, s1
	s_lshl_b32 s1, s17, 22
	s_or_b32 s0, s0, s1
	s_lshr_b32 s1, s17, 10
	s_waitcnt lgkmcnt(0)
	s_add_u32 s12, s12, s0
	s_addc_u32 s13, s13, s1
	s_lshl_b32 s0, s16, 15
	s_lshl_b32 s1, s68, 6
	s_add_u32 s0, s0, s1
	s_lshl_b32 s1, s23, 20
	s_add_u32 s0, s0, s1
	s_add_u32 s0, s0, 0x12400000
	s_mul_i32 s1, s21, 0x1a800000
	s_add_u32 s0, s0, s1
	s_add_u32 s14, s19, s0
	s_addc_u32 s15, s20, 0
	s_mov_b32 s16, 1
.Lbw_dd:
	s_cmp_eq_u32 s16, 0
	s_cselect_b32 s22, 14, 16
	s_cselect_b32 s23, 13, 11
	s_movk_i32 s21, 0x2000
	s_cselect_b32 s21, 0x800, s21
	s_movk_i32 s17, 0x200
	s_cselect_b32 s17, 0x800, s17
	v_mbcnt_lo_u32_b32 v0, -1, 0
	v_mbcnt_hi_u32_b32 v0, -1, v0
	v_lshrrev_b32_e32 v1, 3, v0
	v_and_b32_e32 v2, 7, v0
	v_lshlrev_b32_e32 v3, 4, v2
	v_lshl_add_u32 v3, v1, s22, v3
	v_lshlrev_b32_e32 v7, 3, v1
	v_lshl_add_u32 v7, v2, s23, v7
	s_lshl_b32 s24, s17, 5
	v_mov_b32_e32 v0, v3
	global_load_dwordx4 v[20:23], v0, s[12:13] nt
	v_add_u32_e32 v0, s21, v0
	global_load_dwordx4 v[24:27], v0, s[12:13] nt
	v_add_u32_e32 v0, s21, v0
	global_load_dwordx4 v[28:31], v0, s[12:13] nt
	v_add_u32_e32 v0, s21, v0
	global_load_dwordx4 v[32:35], v0, s[12:13] nt
	v_add_u32_e32 v0, s21, v0
	global_load_dwordx4 v[36:39], v0, s[12:13] nt
	v_add_u32_e32 v0, s21, v0
	global_load_dwordx4 v[40:43], v0, s[12:13] nt
	v_add_u32_e32 v0, s21, v0
	global_load_dwordx4 v[44:47], v0, s[12:13] nt
	v_add_u32_e32 v0, s21, v0
	global_load_dwordx4 v[48:51], v0, s[12:13] nt
	s_waitcnt vmcnt(0)
; #define LAS __attribute__((address_space(3)))
; __device__ __forceinline__ float clamp8(float x) { return __builtin_amdgcn_fmed3f(x, -448.f, 448.f); }
; #define LDS_WAIT() asm volatile("s_waitcnt lgkmcnt(0)" ::: "memory")
; __device__ __forceinline__ void cvt_finish(const CvtDesc& d, const float (&t)[64], LAS float* scr, int lane) {
;     LAS float* sw = scr + (lane >> 4) * 65 + 4 * (lane & 15);
; #pragma unroll
;     for (int i = 0; i < 16; ++i) { sw[(4 * i) * 65] = t[4 * i]; sw[(4 * i) * 65 + 1] = t[4 * i + 1]; sw[(4 * i) * 65 + 2] = t[4 * i + 2]; sw[(4 * i) * 65 + 3] = t[4 * i + 3]; }
;     LDS_WAIT();
;     const int c = lane & 7;
;     if (d.f8) {
; #pragma unroll
;         for (int j = 0; j < 8; ++j) { const int n = (lane >> 3) + 8 * j; const LAS float* s = scr + (8 * c) * 65 + n;
;             int a = __builtin_amdgcn_cvt_pk_fp8_f32(clamp8(s[0 * 65] * W8_SCALE), clamp8(s[1 * 65] * W8_SCALE), 0, false); a = __builtin_amdgcn_cvt_pk_fp8_f32(clamp8(s[2 * 65] * W8_SCALE), clamp8(s[3 * 65] * W8_SCALE), a, true);
;             int b = __builtin_amdgcn_cvt_pk_fp8_f32(clamp8(s[4 * 65] * W8_SCALE), clamp8(s[5 * 65] * W8_SCALE), 0, false); b = __builtin_amdgcn_cvt_pk_fp8_f32(clamp8(s[6 * 65] * W8_SCALE), clamp8(s[7 * 65] * W8_SCALE), b, true);
;             __builtin_nontemporal_store((u32x2){(unsigned)a, (unsigned)b}, (u32x2*)(d.dst + (size_t)n * d.dKB + 8 * c)); }
	v_mul_f32_e32 v20, 0x42800000, v20
	v_mul_f32_e32 v21, 0x42800000, v21
	v_mul_f32_e32 v22, 0x42800000, v22
	v_mul_f32_e32 v23, 0x42800000, v23
	v_mul_f32_e32 v24, 0x42800000, v24
	v_mul_f32_e32 v25, 0x42800000, v25
	v_mul_f32_e32 v26, 0x42800000, v26
	v_mul_f32_e32 v27, 0x42800000, v27
	v_mul_f32_e32 v28, 0x42800000, v28
	v_mul_f32_e32 v29, 0x42800000, v29
	v_mul_f32_e32 v30, 0x42800000, v30
	v_mul_f32_e32 v31, 0x42800000, v31
	v_mul_f32_e32 v32, 0x42800000, v32
	v_mul_f32_e32 v33, 0x42800000, v33
	v_mul_f32_e32 v34, 0x42800000, v34
	v_mul_f32_e32 v35, 0x42800000, v35
	v_mul_f32_e32 v36, 0x42800000, v36
	v_mul_f32_e32 v37, 0x42800000, v37
	v_mul_f32_e32 v38, 0x42800000, v38
	v_mul_f32_e32 v39, 0x42800000, v39
	v_mul_f32_e32 v40, 0x42800000, v40
	v_mul_f32_e32 v41, 0x42800000, v41
	v_mul_f32_e32 v42, 0x42800000, v42
	v_mul_f32_e32 v43, 0x42800000, v43
	v_mul_f32_e32 v44, 0x42800000, v44
	v_mul_f32_e32 v45, 0x42800000, v45
	v_mul_f32_e32 v46, 0x42800000, v46
	v_mul_f32_e32 v47, 0x42800000, v47
	v_mul_f32_e32 v48, 0x42800000, v48
	v_mul_f32_e32 v49, 0x42800000, v49
	v_mul_f32_e32 v50, 0x42800000, v50
	v_mul_f32_e32 v51, 0x42800000, v51
	v_med3_f32 v20, v20, s93, v224
	v_med3_f32 v21, v21, s93, v224
	v_med3_f32 v22, v22, s93, v224
	v_med3_f32 v23, v23, s93, v224
	v_med3_f32 v24, v24, s93, v224
	v_med3_f32 v25, v25, s93, v224
	v_med3_f32 v26, v26, s93, v224
	v_med3_f32 v27, v27, s93, v224
	v_med3_f32 v28, v28, s93, v224
	v_med3_f32 v29, v29, s93, v224
	v_med3_f32 v30, v30, s93, v224
	v_med3_f32 v31, v31, s93, v224
	v_med3_f32 v32, v32, s93, v224
	v_med3_f32 v33, v33, s93, v224
	v_med3_f32 v34, v34, s93, v224
	v_med3_f32 v35, v35, s93, v224
	v_med3_f32 v36, v36, s93, v224
	v_med3_f32 v37, v37, s93, v224
	v_med3_f32 v38, v38, s93, v224
	v_med3_f32 v39, v39, s93, v224
	v_med3_f32 v40, v40, s93, v224
	v_med3_f32 v41, v41, s93, v224
	v_med3_f32 v42, v42, s93, v224
	v_med3_f32 v43, v43, s93, v224
	v_med3_f32 v44, v44, s93, v224
	v_med3_f32 v45, v45, s93, v224
	v_med3_f32 v46, v46, s93, v224
	v_med3_f32 v47, v47, s93, v224
	v_med3_f32 v48, v48, s93, v224
	v_med3_f32 v49, v49, s93, v224
	v_med3_f32 v50, v50, s93, v224
	v_med3_f32 v51, v51, s93, v224
	v_mov_b32_e32 v0, v7
	v_cvt_pk_fp8_f32 v52, v20, v24
	v_cvt_pk_fp8_f32 v53, v36, v40
	v_cvt_pk_fp8_f32 v52, v28, v32 op_sel:[0,0,1]
	v_cvt_pk_fp8_f32 v53, v44, v48 op_sel:[0,0,1]
	s_nop 0
	global_store_dwordx2 v0, v[52:53], s[14:15] nt
	v_add_u32_e32 v0, s17, v0
	v_cvt_pk_fp8_f32 v52, v21, v25
	v_cvt_pk_fp8_f32 v53, v37, v41
	v_cvt_pk_fp8_f32 v52, v29, v33 op_sel:[0,0,1]
	v_cvt_pk_fp8_f32 v53, v45, v49 op_sel:[0,0,1]
	s_nop 0
	global_store_dwordx2 v0, v[52:53], s[14:15] nt
	v_add_u32_e32 v0, s17, v0
	v_cvt_pk_fp8_f32 v52, v22, v26
	v_cvt_pk_fp8_f32 v53, v38, v42
	v_cvt_pk_fp8_f32 v52, v30, v34 op_sel:[0,0,1]
	v_cvt_pk_fp8_f32 v53, v46, v50 op_sel:[0,0,1]
	s_nop 0
	global_store_dwordx2 v0, v[52:53], s[14:15] nt
	v_add_u32_e32 v0, s17, v0
	v_cvt_pk_fp8_f32 v52, v23, v27
	v_cvt_pk_fp8_f32 v53, v39, v43
	v_cvt_pk_fp8_f32 v52, v31, v35 op_sel:[0,0,1]
	v_cvt_pk_fp8_f32 v53, v47, v51 op_sel:[0,0,1]
	s_nop 0
	global_store_dwordx2 v0, v[52:53], s[14:15] nt
	v_add_u32_e32 v0, 0x80, v3
	global_load_dwordx4 v[20:23], v0, s[12:13] nt
	v_add_u32_e32 v0, s21, v0
	global_load_dwordx4 v[24:27], v0, s[12:13] nt
	v_add_u32_e32 v0, s21, v0
	global_load_dwordx4 v[28:31], v0, s[12:13] nt
	v_add_u32_e32 v0, s21, v0
	global_load_dwordx4 v[32:35], v0, s[12:13] nt
	v_add_u32_e32 v0, s21, v0
	global_load_dwordx4 v[36:39], v0, s[12:13] nt
	v_add_u32_e32 v0, s21, v0
	global_load_dwordx4 v[40:43], v0, s[12:13] nt
	v_add_u32_e32 v0, s21, v0
	global_load_dwordx4 v[44:47], v0, s[12:13] nt
	v_add_u32_e32 v0, s21, v0
	global_load_dwordx4 v[48:51], v0, s[12:13] nt
	s_waitcnt vmcnt(0)
	v_mul_f32_e32 v20, 0x42800000, v20
	v_mul_f32_e32 v21, 0x42800000, v21
	v_mul_f32_e32 v22, 0x42800000, v22
	v_mul_f32_e32 v23, 0x42800000, v23
	v_mul_f32_e32 v24, 0x42800000, v24
	v_mul_f32_e32 v25, 0x42800000, v25
	v_mul_f32_e32 v26, 0x42800000, v26
	v_mul_f32_e32 v27, 0x42800000, v27
	v_mul_f32_e32 v28, 0x42800000, v28
	v_mul_f32_e32 v29, 0x42800000, v29
	v_mul_f32_e32 v30, 0x42800000, v30
	v_mul_f32_e32 v31, 0x42800000, v31
	v_mul_f32_e32 v32, 0x42800000, v32
	v_mul_f32_e32 v33, 0x42800000, v33
	v_mul_f32_e32 v34, 0x42800000, v34
	v_mul_f32_e32 v35, 0x42800000, v35
	v_mul_f32_e32 v36, 0x42800000, v36
	v_mul_f32_e32 v37, 0x42800000, v37
	v_mul_f32_e32 v38, 0x42800000, v38
	v_mul_f32_e32 v39, 0x42800000, v39
	v_mul_f32_e32 v40, 0x42800000, v40
	v_mul_f32_e32 v41, 0x42800000, v41
	v_mul_f32_e32 v42, 0x42800000, v42
	v_mul_f32_e32 v43, 0x42800000, v43
	v_mul_f32_e32 v44, 0x42800000, v44
	v_mul_f32_e32 v45, 0x42800000, v45
	v_mul_f32_e32 v46, 0x42800000, v46
	v_mul_f32_e32 v47, 0x42800000, v47
	v_mul_f32_e32 v48, 0x42800000, v48
	v_mul_f32_e32 v49, 0x42800000, v49
	v_mul_f32_e32 v50, 0x42800000, v50
	v_mul_f32_e32 v51, 0x42800000, v51
	v_med3_f32 v20, v20, s93, v224
	v_med3_f32 v21, v21, s93, v224
	v_med3_f32 v22, v22, s93, v224
	v_med3_f32 v23, v23, s93, v224
	v_med3_f32 v24, v24, s93, v224
	v_med3_f32 v25, v25, s93, v224
	v_med3_f32 v26, v26, s93, v224
	v_med3_f32 v27, v27, s93, v224
	v_med3_f32 v28, v28, s93, v224
	v_med3_f32 v29, v29, s93, v224
	v_med3_f32 v30, v30, s93, v224
	v_med3_f32 v31, v31, s93, v224
	v_med3_f32 v32, v32, s93, v224
	v_med3_f32 v33, v33, s93, v224
	v_med3_f32 v34, v34, s93, v224
	v_med3_f32 v35, v35, s93, v224
	v_med3_f32 v36, v36, s93, v224
	v_med3_f32 v37, v37, s93, v224
	v_med3_f32 v38, v38, s93, v224
	v_med3_f32 v39, v39, s93, v224
	v_med3_f32 v40, v40, s93, v224
	v_med3_f32 v41, v41, s93, v224
	v_med3_f32 v42, v42, s93, v224
	v_med3_f32 v43, v43, s93, v224
	v_med3_f32 v44, v44, s93, v224
	v_med3_f32 v45, v45, s93, v224
	v_med3_f32 v46, v46, s93, v224
	v_med3_f32 v47, v47, s93, v224
	v_med3_f32 v48, v48, s93, v224
	v_med3_f32 v49, v49, s93, v224
	v_med3_f32 v50, v50, s93, v224
	v_med3_f32 v51, v51, s93, v224
	v_add_u32_e32 v0, s24, v7
	v_cvt_pk_fp8_f32 v52, v20, v24
	v_cvt_pk_fp8_f32 v53, v36, v40
	v_cvt_pk_fp8_f32 v52, v28, v32 op_sel:[0,0,1]
	v_cvt_pk_fp8_f32 v53, v44, v48 op_sel:[0,0,1]
	s_nop 0
	global_store_dwordx2 v0, v[52:53], s[14:15] nt
	v_add_u32_e32 v0, s17, v0
	v_cvt_pk_fp8_f32 v52, v21, v25
	v_cvt_pk_fp8_f32 v53, v37, v41
	v_cvt_pk_fp8_f32 v52, v29, v33 op_sel:[0,0,1]
	v_cvt_pk_fp8_f32 v53, v45, v49 op_sel:[0,0,1]
	s_nop 0
	global_store_dwordx2 v0, v[52:53], s[14:15] nt
	v_add_u32_e32 v0, s17, v0
	v_cvt_pk_fp8_f32 v52, v22, v26
	v_cvt_pk_fp8_f32 v53, v38, v42
	v_cvt_pk_fp8_f32 v52, v30, v34 op_sel:[0,0,1]
	v_cvt_pk_fp8_f32 v53, v46, v50 op_sel:[0,0,1]
	s_nop 0
	global_store_dwordx2 v0, v[52:53], s[14:15] nt
	v_add_u32_e32 v0, s17, v0
	v_cvt_pk_fp8_f32 v52, v23, v27
	v_cvt_pk_fp8_f32 v53, v39, v43
	v_cvt_pk_fp8_f32 v52, v31, v35 op_sel:[0,0,1]
	v_cvt_pk_fp8_f32 v53, v47, v51 op_sel:[0,0,1]
	s_nop 0
	global_store_dwordx2 v0, v[52:53], s[14:15] nt
	s_branch .LBB0_625
